# P1: GEMM workgroups raise the converters' stop flag two K-loop iterations before the end of their last unit (was: after the epilogue stores drained)
# speedup vs baseline: 1.0022x; 1.0022x over previous
; #define PG8_STAGE(bufoff, gbase, voff) do { _Pragma("unroll") for (int _i = 0; _i < 2; ++_i) \
;         __builtin_amdgcn_global_load_lds((const unsigned*)((const char*)(gbase) + (voff)[_i]), (LAS unsigned*)(lds + (bufoff) + ldsw + _i * 8192), 16, 0, 0); } while (0)
; template <class Epi, class Sched, bool ALIGN_EPI, bool FP8 = false>
; __device__ __forceinline__ void gemm_phase(LAS unsigned char* lds, const Gemm g, const Sched& S, const Epi& E) {
;     ...
;         for (int t = 0; t < nt; t += 2) {
;             const bool last = (t == nt - 2);
;             const char* a1 = Ab + (size_t)(t + 1) * kstep;
;             PG8_LDB(B0, 0, 0); PG8_LDB(B1, 0, 1); PG8_SCHED; PG8_LDA(At, 0, 0); PG8_STAGE(PG8_SA(1, 1), a1, ao[1]);
;             PG8_WAIT_V(8); PG8_WAIT_L(0); PG8_BAR; if (do0) { PG8_MMA(0, 0, At, B0); PG8_MMA(0, 1, At, B1); } PG8_BAR; PG8_SCHED;
;             const char* a2 = last ? Ab : Ab + (size_t)(t + 2) * kstep; const char* b2 = last ? nB : cB + (size_t)(t + 2) * kstep;
;             if (last && has_next) { int t2 = tid; asm volatile("" : "+v"(t2)); int R2[2], C2[2];
; #pragma unroll
;                 for (int i = 0; i < 2; ++i) stage_rc(t2 * 16 + i * 8192, R2[i], C2[i]);
;                 S.a_off_next(nxt, R2, C2, ao, lds + AUX_OFF); }
;             const char* a3 = a2 + kstep; const char* b3 = b2 + kstep;
;             PG8_LDA(At, 0, 1); PG8_STAGE(PG8_SB(0, 0), b2, voffB); PG8_STAGE(PG8_SB(0, 1), b2 + hstep, voffB); PG8_STAGE(PG8_SA(0, 0), a2, ao[0]);
;             PG8_WAIT_V(8); PG8_WAIT_L(0); PG8_BAR; if (full) { PG8_MMA(1, 0, At, B0); PG8_MMA(1, 1, At, B1); } PG8_BAR; PG8_SCHED;
;             PG8_LDB(B0, 1, 0); PG8_LDB(B1, 1, 1); PG8_SCHED; PG8_LDA(At, 1, 0); PG8_STAGE(PG8_SA(0, 1), a2, ao[1]);
;             PG8_WAIT_V(8); PG8_WAIT_L(0); PG8_BAR; if (do0) { PG8_MMA(0, 0, At, B0); PG8_MMA(0, 1, At, B1); } PG8_BAR; PG8_SCHED;
;             PG8_LDA(At, 1, 1); PG8_STAGE(PG8_SB(1, 0), b3, voffB); PG8_STAGE(PG8_SB(1, 1), b3 + hstep, voffB); PG8_STAGE(PG8_SA(1, 0), a3, ao[0]);
;             PG8_WAIT_V(8); PG8_WAIT_L(0); PG8_BAR; if (full) { PG8_MMA(1, 0, At, B0); PG8_MMA(1, 1, At, B1); } PG8_BAR; PG8_SCHED;
;         }
; __device__ __forceinline__ void phase1() { const Ctx c = make_ctx(); PHASE_PTRS;
;     ...
;             const Ctx c3 = make_ctx(); if (c3.tid == 0) __hip_atomic_fetch_add(ctl + CW_PDONE, 1u, __ATOMIC_RELAXED, __HIP_MEMORY_SCOPE_AGENT);
.LBB0_313:
	s_barrier
	s_add_i32 s87, s87, 2
	s_add_u32 s85, s85, 0x100
	s_addc_u32 s86, s86, 0
	s_add_u32 s62, s62, 0x100
	s_addc_u32 s63, s63, 0
	s_cmp_eq_u32 s87, 26
	s_cbranch_scc0 .Lp1sig_skip
	s_and_b64 s[98:99], s[4:5], exec
	s_cbranch_scc1 .Lp1sig_skip
	v_readfirstlane_b32 s98, v0
	s_cmp_lg_u32 s98, 0
	s_cbranch_scc1 .Lp1sig_skip
	s_mov_b64 s[98:99], exec
	s_mov_b64 exec, 1
	v_mov_b32_e32 v253, 0x1000
	v_mov_b32_e32 v254, 1
	global_atomic_add v253, v254, s[30:31] offset:1280
	s_mov_b64 exec, s[98:99]
.Lp1sig_skip:
	s_cmp_gt_u32 s87, 29
	s_cbranch_scc1 .LBB0_324

; #define PG8_WAIT_V(n) asm volatile("s_waitcnt vmcnt(" #n ")" ::: "memory")
; #define PG8_BAR __builtin_amdgcn_s_barrier()
; template <class Epi, class Sched, bool ALIGN_EPI, bool FP8 = false>
; __device__ __forceinline__ void gemm_phase(LAS unsigned char* lds, const Gemm g, const Sched& S, const Epi& E) {
;     ...
;     PG8_WAIT_V(0);
;     S.unit_done(prev_pm, lane);
;     if constexpr (!ALIGN_EPI) { if (wr == 0) PG8_BAR; }
;     PG8_BAR;
; __device__ __forceinline__ void phase1() { const Ctx c = make_ctx(); PHASE_PTRS;
;     ...
;             const Ctx c3 = make_ctx(); if (c3.tid == 0) __hip_atomic_fetch_add(ctl + CW_PDONE, 1u, __ATOMIC_RELAXED, __HIP_MEMORY_SCOPE_AGENT);
.LBB0_329:
	s_waitcnt vmcnt(0)
	v_mov_b32_e32 v1, v0
	s_barrier
	s_nop 0
	v_cmp_eq_u32_e32 vcc, 0, v1
	s_and_saveexec_b64 s[4:5], vcc
	s_cbranch_execz .LBB0_332
	s_mov_b64 s[6:7], exec
	v_mbcnt_lo_u32_b32 v1, s6, 0
	v_mbcnt_hi_u32_b32 v1, s7, v1
	v_cmp_eq_u32_e32 vcc, 0, v1
	s_and_b64 s[8:9], exec, vcc
	s_mov_b64 exec, s[8:9]
	s_cbranch_execz .LBB0_332
	s_bcnt1_i32_b64 s6, s[6:7]
	v_mov_b32_e32 v1, 0x1000
	v_mov_b32_e32 v2, s6
.LBB0_332:
	s_or_b64 exec, exec, s[4:5]

; __global__ void __launch_bounds__(NWAVES * 64, 2) mk_fwd(Args a) {
	.amdhsa_kernel _Z6mk_fwd4Args
		.amdhsa_group_segment_fixed_size 0
		.amdhsa_private_segment_fixed_size 0
		.amdhsa_kernarg_size 440
		.amdhsa_user_sgpr_count 2
		.amdhsa_user_sgpr_dispatch_ptr 0
		.amdhsa_user_sgpr_queue_ptr 0
		.amdhsa_user_sgpr_kernarg_segment_ptr 1
		.amdhsa_user_sgpr_dispatch_id 0
		.amdhsa_user_sgpr_kernarg_preload_length 0
		.amdhsa_user_sgpr_kernarg_preload_offset 0
		.amdhsa_user_sgpr_private_segment_size 0
		.amdhsa_uses_dynamic_stack 0
		.amdhsa_enable_private_segment 0
		.amdhsa_system_sgpr_workgroup_id_x 1
		.amdhsa_system_sgpr_workgroup_id_y 0
		.amdhsa_system_sgpr_workgroup_id_z 0
		.amdhsa_system_sgpr_workgroup_info 0
		.amdhsa_system_vgpr_workitem_id 0
		.amdhsa_next_free_vgpr 255
		.amdhsa_next_free_sgpr 100
		.amdhsa_accum_offset 256
		.amdhsa_reserve_vcc 1
		.amdhsa_float_round_mode_32 0
		.amdhsa_float_round_mode_16_64 0
		.amdhsa_float_denorm_mode_32 3
		.amdhsa_float_denorm_mode_16_64 3
		.amdhsa_dx10_clamp 1
		.amdhsa_ieee_mode 1
		.amdhsa_fp16_overflow 0
		.amdhsa_tg_split 0
		.amdhsa_exception_fp_ieee_invalid_op 0
		.amdhsa_exception_fp_denorm_src 0
		.amdhsa_exception_fp_ieee_div_zero 0
		.amdhsa_exception_fp_ieee_overflow 0
		.amdhsa_exception_fp_ieee_underflow 0
		.amdhsa_exception_fp_ieee_inexact 0
		.amdhsa_exception_int_div_zero 0
	.end_amdhsa_kernel

; __global__ void __launch_bounds__(NWAVES * 64, 2) mk_fwd(Args a) {
amdhsa.kernels:
  - .agpr_count:     0
    .args:
      - .offset:         0
        .size:           184
        .value_kind:     by_value
      - .offset:         184
        .size:           4
        .value_kind:     hidden_block_count_x
      - .offset:         188
        .size:           4
        .value_kind:     hidden_block_count_y
      - .offset:         192
        .size:           4
        .value_kind:     hidden_block_count_z
      - .offset:         196
        .size:           2
        .value_kind:     hidden_group_size_x
      - .offset:         198
        .size:           2
        .value_kind:     hidden_group_size_y
      - .offset:         200
        .size:           2
        .value_kind:     hidden_group_size_z
      - .offset:         202
        .size:           2
        .value_kind:     hidden_remainder_x
      - .offset:         204
        .size:           2
        .value_kind:     hidden_remainder_y
      - .offset:         206
        .size:           2
        .value_kind:     hidden_remainder_z
      - .offset:         224
        .size:           8
        .value_kind:     hidden_global_offset_x
      - .offset:         232
        .size:           8
        .value_kind:     hidden_global_offset_y
      - .offset:         240
        .size:           8
        .value_kind:     hidden_global_offset_z
      - .offset:         248
        .size:           2
        .value_kind:     hidden_grid_dims
      - .offset:         304
        .size:           4
        .value_kind:     hidden_dynamic_lds_size
    .group_segment_fixed_size: 0
    .kernarg_segment_align: 8
    .kernarg_segment_size: 440
    .language:       OpenCL C
    .language_version:
      - 2
      - 0
    .max_flat_workgroup_size: 512
    .name:           _Z6mk_fwd4Args
    .private_segment_fixed_size: 0
    .sgpr_count:     106
    .sgpr_spill_count: 21
    .symbol:         _Z6mk_fwd4Args.kd
    .uniform_work_group_size: 1
    .uses_dynamic_stack: false
    .vgpr_count:     255
    .vgpr_spill_count: 0
    .wavefront_size: 64
